# conversion-in-attention: loop-top wait no longer waits for the conversion stores (vmcnt 7 after a converting iteration)
# speedup vs baseline: 1.0313x; 1.0023x over previous
; #define LAS __attribute__((address_space(3)))
; __device__ __forceinline__ void lds_barrier() { asm volatile("s_waitcnt lgkmcnt(0)\n\ts_barrier" ::: "memory"); }
; __device__ __forceinline__ void phase_attn(Frame& F) {
;     ...
;         lds_barrier();
;         LAS unsigned char* kb = F.lds + buf * ABUF;
;         const bf16x8 q0 = qn0, q1 = qn1;
;         {
;             LAS unsigned char* ob = F.lds + (buf ^ 1) * ABUF;
; #pragma unroll
;             for (int jj = 0; jj < 4; ++jj) { const int ch = tid + 512 * jj, row = ch >> 3, c16 = ch & 7;
;                 *(LAS u32x4*)(ob + row * ATT_ROWB + c16 * 16) = kr[jj]; *(LAS u32x4*)(ob + ATT_VOFF + row * ATT_ROWB + c16 * 16) = vr[jj]; }
;         }
;         const AttnUnit nu = un;
;         un = attn_decode(x8 * PER_X + (jl + 2 * G8 < jlast ? jl + 2 * G8 : jlast)); attn_issue(qkv, un, tid, kr, vr);
;         { const char* qb = (const char*)qkv + (((size_t)nu.b * SEQ + nu.r) * NPROJ + nu.h * 64) * 2; const unsigned qo = __umul24((unsigned)(128 * nu.n + ql), (unsigned)nu.d * (NPROJ * 2)) + 16u * fq;
;           qn0 = *(const bf16x8*)(qb + qo); qn1 = *(const bf16x8*)(qb + qo + 64); }
;         const unsigned qrow = __umul24((unsigned)(128 * cu.n + ql), (unsigned)cu.d);
;         const float c1 = 0.125f * LOG2E;
;         const float nc2 = -__builtin_amdgcn_exp2f(-(float)(cu.h + 1)) * (float)cu.d * LOG2E;
;         const bool first = cu.n == 0;
;         f32x4 St[9];
;         const f32x4 eb = (f32x4){ef[0], ef[1], ef[2], ef[3]} * nc2;
;         float mx = -INFINITY;
;         bf16x8 kf[9][2];
; #pragma unroll
;         for (int T = 0; T < 9; ++T) { LAS unsigned char* ka = kb + (16 * (w + T) + fr) * ATT_ROWB + fq * 16; kf[T][0] = *(LAS bf16x8*)ka; kf[T][1] = *(LAS bf16x8*)(ka + 64); }
.LBB0_304:
	s_mul_i32 s37, s79, 0x12000
	s_add_i32 s85, s37, 0
	s_cmp_eq_u32 s95, 0
	s_cbranch_scc1 .Lcva_w3
	s_waitcnt vmcnt(7)
	s_mov_b32 s95, 0
	s_branch .Lcva_wd
.Lcva_w3:
	s_waitcnt vmcnt(3)
.Lcva_wd:
	v_mov_b64_e32 v[48:49], v[4:5]
	v_mov_b64_e32 v[46:47], v[2:3]
	v_mov_b64_e32 v[44:45], v[8:9]
	v_mov_b64_e32 v[42:43], v[6:7]
	s_lshl_b32 s65, 1, s35
	s_waitcnt lgkmcnt(0)
	s_barrier
	s_add_i32 s37, s30, 1
	v_cvt_f32_u32_e32 v54, s37
	v_cvt_f32_u32_e32 v55, s65
	v_add_u32_e32 v110, s85, v82
	v_add_u32_e32 v58, v110, v90
	v_exp_f32_e64 v54, -v54
	v_add_u32_e32 v66, v110, v91
	v_add_u32_e32 v74, v110, v92
	v_add_u32_e32 v111, v110, v93
	v_mul_f32_e32 v79, v55, v54
	ds_read_b128 v[54:57], v58
	ds_read_b128 v[58:61], v58 offset:64
	ds_read_b128 v[62:65], v66
	ds_read_b128 v[66:69], v66 offset:64
	ds_read_b128 v[70:73], v74
	ds_read_b128 v[74:77], v74 offset:64
	ds_read_b128 v[112:115], v111
	ds_read_b128 v[116:119], v111 offset:64
	v_add_u32_e32 v111, v110, v94
	ds_read_b128 v[120:123], v111
	ds_read_b128 v[124:127], v111 offset:64
	v_add_u32_e32 v111, v110, v95
	ds_read_b128 v[128:131], v111
	ds_read_b128 v[132:135], v111 offset:64
	v_add_u32_e32 v111, v110, v96
	ds_read_b128 v[136:139], v111
	ds_read_b128 v[140:143], v111 offset:64
	v_add_u32_e32 v111, v110, v97
	v_add_u32_e32 v110, v110, v98
	ds_read_b128 v[144:147], v111
	ds_read_b128 v[148:151], v111 offset:64
	ds_read_b128 v[152:155], v110
	ds_read_b128 v[156:159], v110 offset:64
	s_and_b32 s98, s32, 3
	s_add_u32 s32, s32, 1
	s_cmp_eq_u32 s98, 0
	s_cbranch_scc0 .Lcva_none_l
	s_cmp_eq_u32 s90, 0
	s_cbranch_scc1 .Lcva_none_l
	s_sub_u32 s90, s90, 1
	s_lshr_b32 s98, s89, 6
	s_and_b32 s99, s89, 63
	s_mul_hi_u32 s100, s98, 0xaaaaaaab
	s_lshr_b32 s100, s100, 1
	s_mul_i32 s101, s100, 3
	s_sub_u32 s101, s98, s101
	s_cmp_lt_u32 s100, 256
	s_cselect_b32 s98, 0, 3
	s_cselect_b32 s95, s100, 0
	s_add_u32 s98, s98, s101
	s_lshl_b32 s98, s98, 1
	v_readlane_b32 s96, v253, s98
	s_add_u32 s98, s98, 1
	v_readlane_b32 s97, v253, s98
	s_lshl_b32 s95, s95, 20
	s_nop 3
	s_add_u32 s96, s96, s95
	s_addc_u32 s97, s97, 0
	s_cmp_eq_u32 s101, 2
	s_cbranch_scc1 .Lcva_down_l
	s_lshr_b32 s95, s99, 3
	s_and_b32 s99, s99, 7
	s_lshl_b32 s98, s95, 17
	s_add_u32 s96, s96, s98
	s_addc_u32 s97, s97, 0
	s_lshl_b32 s98, s99, 7
	s_add_u32 s96, s96, s98
	s_addc_u32 s97, s97, 0
	s_lshl_b32 s100, s100, 19
	s_lshr_b32 s98, s99, 2
	s_lshl_b32 s98, s98, 18
	s_add_u32 s100, s100, s98
	s_and_b32 s98, s99, 3
	s_lshl_b32 s98, s98, 15
	s_add_u32 s100, s100, s98
	s_lshl_b32 s98, s101, 17
	s_add_u32 s100, s100, s98
	s_lshl_b32 s98, s95, 7
	s_add_u32 s100, s100, s98
	v_readlane_b32 s92, v253, 12
	v_readlane_b32 s93, v253, 13
	s_mov_b32 s94, 0xc3317218
	s_cmp_eq_u32 s101, 0
	s_cselect_b32 s94, 0xc2b8aa3b, s94
	s_nop 3
	s_add_u32 s92, s92, s100
	s_addc_u32 s93, s93, 0
	s_movk_i32 s95, 0x400
	s_movk_i32 s98, 0x400
	s_branch .Lcva_go_l

; __device__ __forceinline__ void phase_attn(Frame& F) {
;     ...
;         for (int T = 0; T < 9; ++T) {
;             f32x4 sa = (f32x4){0.f, 0.f, 0.f, 0.f};
;             sa = __builtin_amdgcn_mfma_f32_16x16x32_bf16(kf[T][0], q0, sa, 0, 0, 0);
;             sa = __builtin_amdgcn_mfma_f32_16x16x32_bf16(kf[T][1], q1, sa, 0, 0, 0);
;             const float kT = (!first || w + T >= 8) ? nc2 * (float)(128 - 16 * T) : -INFINITY;
;             sa = sa * c1 + (eb + kT);
; #pragma unroll
;             for (int rg = 0; rg < 4; ++rg) {
;                 if (T == 0) sa[rg] = ef[rg] <= 0.f ? sa[rg] : -INFINITY;
;                 if (T == 8) sa[rg] = ef[rg] >= 0.f ? sa[rg] : -INFINITY;
;             }
;             St[T] = sa;
;             mx = fmaxf(mx, fmaxf(fmaxf(sa[0], sa[1]), fmaxf(sa[2], sa[3])));
.Lcva_none_l:
	s_cmp_lg_u32 s64, 0
	v_lshl_add_u32 v78, s64, 7, v86
	s_cselect_b64 s[64:65], -1, 0
	v_mul_f32_e32 v160, 0xbfb8aa3b, v79
	v_and_b32_e32 v110, 0xffffff, v78
	s_waitcnt lgkmcnt(14)
	v_mfma_f32_16x16x32_bf16 v[54:57], v[54:57], v[46:49], 0
	v_mul_f32_e32 v78, 0x43000000, v160
	s_or_b64 vcc, s[64:65], s[38:39]
	v_cndmask_b32_e32 v78, v109, v78, vcc
	v_mfma_f32_16x16x32_bf16 v[54:57], v[58:61], v[42:45], v[54:57]
	v_fma_f32 v162, v50, v160, v78
	v_fma_f32 v163, v51, v160, v78
	v_pk_fma_f32 v[78:79], v[52:53], v[160:161], v[78:79] op_sel_hi:[1,0,0]
	s_or_b64 vcc, s[64:65], s[40:41]
	s_nop 3
	v_pk_fma_f32 v[56:57], v[56:57], s[56:57], v[78:79] op_sel_hi:[1,0,1]
	v_pk_fma_f32 v[54:55], v[54:55], s[56:57], v[162:163] op_sel_hi:[1,0,1]
	v_cndmask_b32_e64 v164, v109, v56, s[10:11]
	v_cndmask_b32_e64 v162, v109, v54, s[6:7]
	v_cndmask_b32_e64 v163, v109, v55, s[8:9]
	v_cndmask_b32_e64 v165, v109, v57, s[12:13]
	v_mfma_f32_16x16x32_bf16 v[54:57], v[62:65], v[46:49], 0
	v_max_f32_e32 v58, v162, v163
	v_max_f32_e32 v59, v164, v165
	v_max3_f32 v62, v58, v59, s78
	v_mfma_f32_16x16x32_bf16 v[54:57], v[66:69], v[42:45], v[54:57]
	v_mul_f32_e32 v58, 0x42e00000, v160
	v_cndmask_b32_e32 v58, v109, v58, vcc
	v_pk_fma_f32 v[60:61], v[50:51], v[160:161], v[58:59] op_sel_hi:[1,0,0]
	v_pk_fma_f32 v[58:59], v[52:53], v[160:161], v[58:59] op_sel_hi:[1,0,0]
	s_or_b64 vcc, s[64:65], s[42:43]
	s_nop 2
	v_pk_fma_f32 v[166:167], v[56:57], s[56:57], v[58:59] op_sel_hi:[1,0,1]
	s_waitcnt lgkmcnt(13)
	v_mfma_f32_16x16x32_bf16 v[56:59], v[70:73], v[46:49], 0
	v_fma_f32 v78, v54, s56, v60
	v_fma_f32 v79, v55, s56, v61
	v_max_f32_e32 v54, v166, v167
	v_max3_f32 v63, v78, v79, v54
	s_waitcnt lgkmcnt(12)
	v_mfma_f32_16x16x32_bf16 v[54:57], v[74:77], v[42:45], v[56:59]
	s_nop 2
	v_mul_f32_e32 v58, 0x42c00000, v160
	v_cndmask_b32_e32 v58, v109, v58, vcc
	v_pk_fma_f32 v[60:61], v[50:51], v[160:161], v[58:59] op_sel_hi:[1,0,0]
	v_pk_fma_f32 v[58:59], v[52:53], v[160:161], v[58:59] op_sel_hi:[1,0,0]
	s_nop 0
	v_pk_fma_f32 v[76:77], v[54:55], s[56:57], v[60:61] op_sel_hi:[1,0,1]
	v_pk_fma_f32 v[74:75], v[56:57], s[56:57], v[58:59] op_sel_hi:[1,0,1]
	s_waitcnt lgkmcnt(11)
	v_mfma_f32_16x16x32_bf16 v[54:57], v[112:115], v[46:49], 0
	v_max_f32_e32 v58, v74, v75
	v_max3_f32 v58, v76, v77, v58
	v_max3_f32 v62, v62, v63, v58
	s_waitcnt lgkmcnt(10)
	v_mfma_f32_16x16x32_bf16 v[54:57], v[116:119], v[42:45], v[54:57]
	v_mul_f32_e32 v58, 0x42a00000, v160
	s_or_b64 vcc, s[64:65], s[44:45]
	v_cndmask_b32_e32 v58, v109, v58, vcc
	v_pk_fma_f32 v[60:61], v[50:51], v[160:161], v[58:59] op_sel_hi:[1,0,0]
	v_pk_fma_f32 v[58:59], v[52:53], v[160:161], v[58:59] op_sel_hi:[1,0,0]
	s_nop 2
	v_pk_fma_f32 v[72:73], v[54:55], s[56:57], v[60:61] op_sel_hi:[1,0,1]
	v_pk_fma_f32 v[70:71], v[56:57], s[56:57], v[58:59] op_sel_hi:[1,0,1]
	s_waitcnt lgkmcnt(9)
	v_mfma_f32_16x16x32_bf16 v[56:59], v[120:123], v[46:49], 0
	v_max_f32_e32 v54, v70, v71
	v_max3_f32 v63, v72, v73, v54
	s_or_b64 vcc, s[64:65], s[46:47]
	s_waitcnt lgkmcnt(8)
	v_mfma_f32_16x16x32_bf16 v[54:57], v[124:127], v[42:45], v[56:59]
	s_nop 2
	v_mul_f32_e32 v58, 0x42800000, v160
	v_cndmask_b32_e32 v58, v109, v58, vcc
	v_pk_fma_f32 v[60:61], v[50:51], v[160:161], v[58:59] op_sel_hi:[1,0,0]
	v_pk_fma_f32 v[58:59], v[52:53], v[160:161], v[58:59] op_sel_hi:[1,0,0]
	s_nop 0
	v_pk_fma_f32 v[68:69], v[54:55], s[56:57], v[60:61] op_sel_hi:[1,0,1]
	v_pk_fma_f32 v[66:67], v[56:57], s[56:57], v[58:59] op_sel_hi:[1,0,1]
	s_waitcnt lgkmcnt(7)
	v_mfma_f32_16x16x32_bf16 v[54:57], v[128:131], v[46:49], 0
	v_max_f32_e32 v58, v66, v67
	v_max3_f32 v58, v68, v69, v58
	v_max3_f32 v111, v62, v63, v58
	s_waitcnt lgkmcnt(6)
	v_mfma_f32_16x16x32_bf16 v[54:57], v[132:135], v[42:45], v[54:57]
	v_mul_f32_e32 v58, 0x42400000, v160
	s_or_b64 vcc, s[64:65], s[48:49]
	v_cndmask_b32_e32 v58, v109, v58, vcc
	v_pk_fma_f32 v[60:61], v[50:51], v[160:161], v[58:59] op_sel_hi:[1,0,0]
	v_pk_fma_f32 v[58:59], v[52:53], v[160:161], v[58:59] op_sel_hi:[1,0,0]
	s_nop 2
	v_pk_fma_f32 v[64:65], v[54:55], s[56:57], v[60:61] op_sel_hi:[1,0,1]
	v_pk_fma_f32 v[62:63], v[56:57], s[56:57], v[58:59] op_sel_hi:[1,0,1]
	s_waitcnt lgkmcnt(5)
	v_mfma_f32_16x16x32_bf16 v[56:59], v[136:139], v[46:49], 0
	v_max_f32_e32 v54, v62, v63
	v_max3_f32 v112, v64, v65, v54
	s_or_b64 vcc, s[64:65], s[50:51]
	s_waitcnt lgkmcnt(4)
	v_mfma_f32_16x16x32_bf16 v[54:57], v[140:143], v[42:45], v[56:59]
	s_nop 2
	v_mul_f32_e32 v58, 0x42000000, v160
	v_cndmask_b32_e32 v58, v109, v58, vcc
	v_pk_fma_f32 v[60:61], v[50:51], v[160:161], v[58:59] op_sel_hi:[1,0,0]
	v_pk_fma_f32 v[58:59], v[52:53], v[160:161], v[58:59] op_sel_hi:[1,0,0]
	s_nop 0
	v_pk_fma_f32 v[60:61], v[54:55], s[56:57], v[60:61] op_sel_hi:[1,0,1]
	v_pk_fma_f32 v[58:59], v[56:57], s[56:57], v[58:59] op_sel_hi:[1,0,1]
	s_waitcnt lgkmcnt(3)
	v_mfma_f32_16x16x32_bf16 v[54:57], v[144:147], v[46:49], 0
	v_max_f32_e32 v113, v58, v59
	v_max3_f32 v113, v60, v61, v113
	v_max3_f32 v111, v111, v112, v113
	s_waitcnt lgkmcnt(1)
	v_mfma_f32_16x16x32_bf16 v[46:49], v[152:155], v[46:49], 0
	s_or_b64 vcc, s[64:65], s[52:53]
	v_add_u32_e32 v144, s85, v89
	v_add_u32_e32 v130, v144, v99
	v_mfma_f32_16x16x32_bf16 v[112:115], v[148:151], v[42:45], v[54:57]
	v_add_u32_e32 v140, v144, v100
	v_add_u32_e32 v145, v144, v101
	s_nop 0
	v_mul_f32_e32 v54, 0x41800000, v160
	s_waitcnt lgkmcnt(0)
; #define LAS __attribute__((address_space(3)))
; __device__ __forceinline__ void phase_attn(Frame& F) {
;     ...
;             LAS unsigned char* ob = F.lds + (buf ^ 1) * ABUF;
; #pragma unroll
;             for (int jj = 0; jj < 4; ++jj) { const int ch = tid + 512 * jj, row = ch >> 3, c16 = ch & 7;
;                 *(LAS u32x4*)(ob + row * ATT_ROWB + c16 * 16) = kr[jj]; *(LAS u32x4*)(ob + ATT_VOFF + row * ATT_ROWB + c16 * 16) = vr[jj]; }
;         }
;         const AttnUnit nu = un;
;         un = attn_decode(x8 * PER_X + (jl + 2 * G8 < jlast ? jl + 2 * G8 : jlast)); attn_issue(qkv, un, tid, kr, vr);
;         { const char* qb = (const char*)qkv + (((size_t)nu.b * SEQ + nu.r) * NPROJ + nu.h * 64) * 2; const unsigned qo = __umul24((unsigned)(128 * nu.n + ql), (unsigned)nu.d * (NPROJ * 2)) + 16u * fq;
;           qn0 = *(const bf16x8*)(qb + qo); qn1 = *(const bf16x8*)(qb + qo + 64); }
;     ...
;             const float kT = (!first || w + T >= 8) ? nc2 * (float)(128 - 16 * T) : -INFINITY;
;             sa = sa * c1 + (eb + kT);
; #pragma unroll
;             for (int rg = 0; rg < 4; ++rg) {
;                 if (T == 0) sa[rg] = ef[rg] <= 0.f ? sa[rg] : -INFINITY;
;                 if (T == 8) sa[rg] = ef[rg] >= 0.f ? sa[rg] : -INFINITY;
;             }
;             St[T] = sa;
;             mx = fmaxf(mx, fmaxf(fmaxf(sa[0], sa[1]), fmaxf(sa[2], sa[3])));
;         }
;         mx = fmaxf(mx, __shfl_xor(mx, 16)); mx = fmaxf(mx, __shfl_xor(mx, 32));
;         f32x4 lv = (f32x4){0.f, 0.f, 0.f, 0.f};
;         f32x4 nmx = (f32x4){-mx, -mx, -mx, -mx}; asm volatile("" : "+v"(nmx));
; #pragma unroll
;         for (int T = 0; T < 9; ++T) { const f32x4 d = St[T] + nmx; f32x4 pv; pv.x = fast_exp2(d.x); pv.y = fast_exp2(d.y); pv.z = fast_exp2(d.z); pv.w = fast_exp2(d.w); St[T] = pv; lv = lv + pv; }
;         float l = (lv.x + lv.y) + (lv.z + lv.w);
;         l += __shfl_xor(l, 16); l += __shfl_xor(l, 32);
;         f32x4 O[4];
; #pragma unroll
;         for (int dt = 0; dt < 4; ++dt) O[dt] = (f32x4){0.f, 0.f, 0.f, 0.f};
; #pragma unroll
;         for (int T = 0; T < 9; ++T) {
;             u32x2 pw; pw.x = cvt_pk_bf16(St[T][0], St[T][1]); pw.y = cvt_pk_bf16(St[T][2], St[T][3]);
;             const s16x4 pb = __builtin_bit_cast(s16x4, pw);
;             LAS unsigned char* va = kb + ATT_VOFF + (16 * (w + T) + 4 * fq + (fr >> 2)) * ATT_ROWB + (8 * (fr & 3)) * 2;
; #pragma unroll
	v_mfma_f32_16x16x32_bf16 v[42:45], v[156:159], v[42:45], v[46:49]
	s_add_i32 s37, s77, s70
	s_xor_b32 s79, s79, 1
	s_min_i32 s37, s37, s71
	s_mul_i32 s58, s79, 0x12000
	s_add_i32 s37, s37, s3
	v_add_u32_e32 v2, s58, v84
	s_mul_hi_i32 s58, s37, 0x2aaaaaab
	s_lshr_b32 s59, s58, 31
	s_ashr_i32 s58, s58, 4
	s_add_i32 s59, s58, s59
	s_mul_i32 s58, s59, 0x60
	s_sub_i32 s37, s37, s58
	s_ashr_i32 s58, s59, 3
	s_and_b32 s80, s59, 7
	v_add_u32_e32 v3, v2, v83
	s_cmp_gt_i32 s37, 31
	ds_write_b128 v3, v[38:41]
	ds_write_b128 v3, v[34:37] offset:36864
	v_add_u32_e32 v3, v2, v85
	s_cselect_b64 s[82:83], -1, 0
	s_cmp_gt_i32 s37, 63
	ds_write_b128 v3, v[30:33]
	ds_write_b128 v3, v[26:29] offset:36864
	v_add_u32_e32 v3, v2, v87
	v_add_u32_e32 v2, v2, v88
	s_cselect_b64 s[86:87], -1, 0
	ds_write_b128 v3, v[22:25]
	ds_write_b128 v3, v[18:21] offset:36864
	ds_write_b128 v2, v[14:17]
	ds_write_b128 v2, v[10:13] offset:36864
	v_cndmask_b32_e64 v2, 0, 1, s[86:87]
	s_cmp_lg_u64 s[82:83], 0
	v_readfirstlane_b32 s59, v2
	s_addc_u32 s81, s59, 0
	s_lshl_b32 s59, s81, 5
	s_lshl_b32 s82, s81, 1
	s_sub_i32 s37, s37, s59
	s_sub_i32 s59, 5, s82
	s_ashr_i32 s83, s37, s59
	s_lshl_b32 s59, -1, s59
	s_andn2_b32 s84, s37, s59
	s_ashr_i32 s59, s58, 31
	s_lshl_b64 s[86:87], s[58:59], 12
	s_ashr_i32 s37, s83, 31
	s_add_u32 s59, s86, s83
	s_addc_u32 s37, s87, s37
	s_mulk_i32 s37, 0xa00
	s_mul_hi_u32 s86, s59, 0xa00
	s_add_i32 s87, s86, s37
	s_mulk_i32 s59, 0xa00
	s_lshl_b32 s37, s80, 6
	s_or_b32 s86, s59, s37
	s_lshl_b64 s[86:87], s[86:87], 1
	s_add_u32 s37, s33, s86
	s_addc_u32 s59, s66, s87
	s_add_u32 s86, s37, 0x400
	s_addc_u32 s87, s59, 0
	s_lshl_b32 s59, s84, 7
	v_add_u32_e32 v2, s59, v81
	s_lshl_b32 s37, 0x1400, s82
	v_max_i32_e32 v3, 0, v2
	v_mul_u32_u24_e32 v3, s37, v3
	v_or_b32_e32 v3, v3, v80
	global_load_dwordx4 v[38:41], v3, s[86:87]
	global_load_dwordx4 v[34:37], v3, s[86:87] offset:1024
	v_max_i32_e32 v3, 0xffffffc0, v2
	v_add_u32_e32 v3, 64, v3
	v_mul_u32_u24_e32 v3, s37, v3
	v_or_b32_e32 v3, v3, v80
	global_load_dwordx4 v[30:33], v3, s[86:87]
	global_load_dwordx4 v[26:29], v3, s[86:87] offset:1024
	v_add_u32_e32 v3, s59, v1
	v_max_i32_e32 v2, 0xffffff40, v2
	v_max_i32_e32 v3, 0, v3
	v_add_u32_e32 v2, 0xc0, v2
	v_mul_u32_u24_e32 v3, s37, v3
	v_mul_u32_u24_e32 v2, s37, v2
	v_or_b32_e32 v3, v3, v80
	v_or_b32_e32 v2, v2, v80
	s_ashr_i32 s37, s36, 31
	global_load_dwordx4 v[22:25], v3, s[86:87]
	global_load_dwordx4 v[18:21], v3, s[86:87] offset:1024
	global_load_dwordx4 v[14:17], v2, s[86:87]
	global_load_dwordx4 v[10:13], v2, s[86:87] offset:1024
	s_lshl_b64 s[86:87], s[36:37], 12
	s_ashr_i32 s37, s73, 31
	s_add_u32 s59, s86, s73
	s_addc_u32 s37, s87, s37
	s_mulk_i32 s37, 0xa00
	s_mul_hi_u32 s86, s59, 0xa00
	s_add_i32 s87, s86, s37
	s_mulk_i32 s59, 0xa00
	s_lshl_b32 s37, s75, 6
	s_or_b32 s86, s59, s37
	s_lshl_b64 s[86:87], s[86:87], 1
	s_add_u32 s86, s33, s86
	s_addc_u32 s87, s66, s87
	s_lshl_b32 s37, 0x1400, s74
	v_lshl_add_u32 v2, s76, 7, v86
	s_and_b32 s37, s37, 0x555400
	v_mul_u32_u24_e32 v2, s37, v2
	v_or_b32_e32 v6, v2, v82
	global_load_dwordx4 v[2:5], v6, s[86:87]
	s_nop 0
	global_load_dwordx4 v[6:9], v6, s[86:87] offset:64
	v_cndmask_b32_e32 v54, v109, v54, vcc
	s_or_b64 vcc, s[64:65], s[54:55]
	v_pk_fma_f32 v[56:57], v[50:51], v[160:161], v[54:55] op_sel_hi:[1,0,0]
	v_mul_f32_e32 v46, 0, v160
	v_cndmask_b32_e32 v46, v109, v46, vcc
	v_pk_fma_f32 v[48:49], v[50:51], v[160:161], v[46:47] op_sel_hi:[1,0,0]
	v_pk_fma_f32 v[46:47], v[52:53], v[160:161], v[46:47] op_sel_hi:[1,0,0]
	v_pk_fma_f32 v[54:55], v[52:53], v[160:161], v[54:55] op_sel_hi:[1,0,0]
	v_pk_fma_f32 v[44:45], v[44:45], s[56:57], v[46:47] op_sel_hi:[1,0,1]
	v_pk_fma_f32 v[42:43], v[42:43], s[56:57], v[48:49] op_sel_hi:[1,0,1]
	v_cndmask_b32_e64 v48, v109, v44, s[18:19]
	v_and_b32_e32 v44, 64, v108
	v_pk_fma_f32 v[54:55], v[114:115], s[56:57], v[54:55] op_sel_hi:[1,0,1]
	v_cndmask_b32_e64 v47, v109, v43, s[16:17]
	v_cndmask_b32_e64 v49, v109, v45, s[20:21]
	v_xor_b32_e32 v43, 16, v108
	v_add_u32_e32 v44, 64, v44
	v_pk_fma_f32 v[56:57], v[112:113], s[56:57], v[56:57] op_sel_hi:[1,0,1]
	v_max_f32_e32 v112, v54, v55
	v_cndmask_b32_e64 v46, v109, v42, s[14:15]
	v_max_f32_e32 v42, v48, v49
	v_cmp_lt_i32_e32 vcc, v43, v44
	v_max3_f32 v112, v56, v57, v112
	v_max3_f32 v42, v46, v47, v42
	v_cndmask_b32_e32 v43, v108, v43, vcc
	v_max3_f32 v42, v111, v112, v42
	v_lshlrev_b32_e32 v142, 2, v43
	ds_bpermute_b32 v43, v142, v42
	s_waitcnt lgkmcnt(0)
	v_max_f32_e32 v43, v43, v43
	v_max_f32_e32 v42, v42, v43
	v_xor_b32_e32 v43, 32, v108
	v_cmp_lt_i32_e32 vcc, v43, v44
	s_nop 1
	v_cndmask_b32_e32 v43, v108, v43, vcc
	v_lshlrev_b32_e32 v143, 2, v43
	ds_bpermute_b32 v43, v143, v42
	s_waitcnt lgkmcnt(0)
	v_max_f32_e32 v43, v43, v43
	v_max_f32_e32 v111, v42, v43
	v_xor_b32_e32 v42, 0x80000000, v111
	v_mov_b32_e32 v43, v42
	v_mov_b32_e32 v44, v42
	v_mov_b32_e32 v45, v42
	ds_read_b64_tr_b16 v[120:121], v130 offset:36864
	v_pk_add_f32 v[118:119], v[166:167], v[44:45]
	v_pk_add_f32 v[112:113], v[164:165], v[44:45]
	v_exp_f32_e32 v126, v118
	v_exp_f32_e32 v127, v119
	ds_read_b64_tr_b16 v[118:119], v130 offset:36872
	v_pk_add_f32 v[114:115], v[162:163], v[42:43]
	v_exp_f32_e32 v112, v112
	v_exp_f32_e32 v114, v114
	v_exp_f32_e32 v113, v113
	v_exp_f32_e32 v115, v115
	ds_read_b64_tr_b16 v[128:129], v130 offset:36928
	ds_read_b64_tr_b16 v[130:131], v130 offset:36936
	v_pk_add_f32 v[134:135], v[76:77], v[42:43]
	v_cvt_pk_bf16_f32 v123, v112, v113
	v_cvt_pk_bf16_f32 v122, v114, v115
	v_pk_add_f32 v[116:117], v[112:113], 0 op_sel_hi:[1,0]
	v_pk_add_f32 v[124:125], v[114:115], 0 op_sel_hi:[1,0]
	s_waitcnt lgkmcnt(3)
; #define LAS __attribute__((address_space(3)))
; __device__ __forceinline__ unsigned cvt_pk_bf16(float lo, float hi) { const f32x2_t v = {lo, hi}; return __builtin_bit_cast(unsigned, __builtin_convertvector(v, bf16x2_t)); }
; __device__ __forceinline__ float fast_exp2(float x) { return __builtin_amdgcn_exp2f(x); }
; __device__ __forceinline__ s16x4 tr_read(LAS unsigned char* p) { return __builtin_bit_cast(s16x4, __builtin_amdgcn_ds_read_tr16_b64_v4i16((LAS s16x4*)p)); }
; __device__ __forceinline__ void phase_attn(Frame& F) {
;     ...
;         for (int T = 0; T < 9; ++T) { const f32x4 d = St[T] + nmx; f32x4 pv; pv.x = fast_exp2(d.x); pv.y = fast_exp2(d.y); pv.z = fast_exp2(d.z); pv.w = fast_exp2(d.w); St[T] = pv; lv = lv + pv; }
;         float l = (lv.x + lv.y) + (lv.z + lv.w);
;         l += __shfl_xor(l, 16); l += __shfl_xor(l, 32);
;         f32x4 O[4];
; #pragma unroll
;         for (int dt = 0; dt < 4; ++dt) O[dt] = (f32x4){0.f, 0.f, 0.f, 0.f};
; #pragma unroll
;         for (int T = 0; T < 9; ++T) {
;             u32x2 pw; pw.x = cvt_pk_bf16(St[T][0], St[T][1]); pw.y = cvt_pk_bf16(St[T][2], St[T][3]);
;             const s16x4 pb = __builtin_bit_cast(s16x4, pw);
;             LAS unsigned char* va = kb + ATT_VOFF + (16 * (w + T) + 4 * fq + (fr >> 2)) * ATT_ROWB + (8 * (fr & 3)) * 2;
; #pragma unroll
;             for (int dt = 0; dt < 4; ++dt) O[dt] = __builtin_amdgcn_mfma_f32_16x16x16bf16_1k(tr_read(va + 64 * (dt >> 1) + 8 * (dt & 1)), pb, O[dt], 0, 0, 0);
	v_mfma_f32_16x16x16_bf16 v[112:115], v[120:121], v[122:123], 0
	v_add_f32_e64 v120, v74, v44
	v_add_f32_e64 v121, v75, v45
	v_pk_add_f32 v[132:133], v[126:127], v[116:117]
	v_exp_f32_e32 v136, v120
	s_waitcnt lgkmcnt(2)
	v_mfma_f32_16x16x16_bf16 v[116:119], v[118:119], v[122:123], 0
	v_exp_f32_e32 v137, v121
	v_pk_add_f32 v[78:79], v[78:79], v[42:43]
	v_cvt_pk_bf16_f32 v139, v126, v127
	s_waitcnt lgkmcnt(1)
	v_mfma_f32_16x16x16_bf16 v[74:77], v[128:129], v[122:123], 0
	ds_read_b64_tr_b16 v[128:129], v140 offset:36864
	v_exp_f32_e32 v78, v78
	v_exp_f32_e32 v79, v79
	s_waitcnt lgkmcnt(1)
	v_mfma_f32_16x16x16_bf16 v[120:123], v[130:131], v[122:123], 0
	ds_read_b64_tr_b16 v[130:131], v140 offset:36872
	ds_read_b64_tr_b16 v[126:127], v140 offset:36928
	ds_read_b64_tr_b16 v[140:141], v140 offset:36936
	v_cvt_pk_bf16_f32 v138, v78, v79
	v_exp_f32_e32 v134, v134
	v_exp_f32_e32 v135, v135
	s_waitcnt lgkmcnt(3)
	v_mfma_f32_16x16x16_bf16 v[112:115], v[128:129], v[138:139], v[112:115]
	v_add_f32_e64 v128, v70, v44
	v_add_f32_e64 v129, v71, v45
	v_pk_add_f32 v[78:79], v[78:79], v[124:125]
	v_pk_add_f32 v[124:125], v[136:137], v[132:133]
	s_waitcnt lgkmcnt(2)
	v_mfma_f32_16x16x16_bf16 v[116:119], v[130:131], v[138:139], v[116:119]
	v_add_f32_e64 v130, v72, v42
	v_add_f32_e64 v131, v73, v43
	v_pk_add_f32 v[78:79], v[134:135], v[78:79]
	v_exp_f32_e32 v128, v128
	s_waitcnt lgkmcnt(1)
	v_mfma_f32_16x16x16_bf16 v[70:73], v[126:127], v[138:139], v[74:77]
	ds_read_b64_tr_b16 v[126:127], v145 offset:36864
	v_exp_f32_e32 v129, v129
	v_pk_add_f32 v[48:49], v[44:45], v[48:49]
	s_waitcnt lgkmcnt(1)
	v_mfma_f32_16x16x16_bf16 v[74:77], v[140:141], v[138:139], v[120:123]
	v_add_f32_e64 v124, v128, v124
	v_add_f32_e64 v125, v129, v125
	s_nop 0
	ds_read_b64_tr_b16 v[120:121], v145 offset:36872
	v_cvt_pk_bf16_f32 v122, v134, v135
	ds_read_b64_tr_b16 v[132:133], v145 offset:36928
	ds_read_b64_tr_b16 v[134:135], v145 offset:36936
	v_cvt_pk_bf16_f32 v123, v136, v137
	v_add_u32_e32 v136, v144, v102
	s_waitcnt lgkmcnt(3)
	v_mfma_f32_16x16x16_bf16 v[112:115], v[126:127], v[122:123], v[112:115]
	v_exp_f32_e32 v126, v130
	v_exp_f32_e32 v127, v131
	v_pk_add_f32 v[130:131], v[68:69], v[42:43]
	s_waitcnt lgkmcnt(2)
	v_mfma_f32_16x16x16_bf16 v[116:119], v[120:121], v[122:123], v[116:119]
	v_add_f32_e64 v120, v66, v44
	v_add_f32_e64 v121, v67, v45
	v_pk_add_f32 v[78:79], v[126:127], v[78:79]
	v_exp_f32_e32 v130, v130
	s_waitcnt lgkmcnt(1)
	v_mfma_f32_16x16x16_bf16 v[66:69], v[132:133], v[122:123], v[70:73]
	ds_read_b64_tr_b16 v[132:133], v136 offset:36864
	v_exp_f32_e32 v120, v120
	v_exp_f32_e32 v121, v121
	s_waitcnt lgkmcnt(1)
	v_mfma_f32_16x16x16_bf16 v[70:73], v[134:135], v[122:123], v[74:77]
	ds_read_b64_tr_b16 v[122:123], v136 offset:36872
	v_cvt_pk_bf16_f32 v134, v126, v127
	v_cvt_pk_bf16_f32 v135, v128, v129
	ds_read_b64_tr_b16 v[128:129], v136 offset:36928
	ds_read_b64_tr_b16 v[136:137], v136 offset:36936
	s_waitcnt lgkmcnt(3)
	v_mfma_f32_16x16x16_bf16 v[74:77], v[132:133], v[134:135], v[112:115]
	v_add_u32_e32 v132, v144, v103
	ds_read_b64_tr_b16 v[126:127], v132 offset:36872
	v_exp_f32_e32 v131, v131
	s_waitcnt lgkmcnt(3)
	v_mfma_f32_16x16x16_bf16 v[112:115], v[122:123], v[134:135], v[116:119]
	ds_read_b64_tr_b16 v[122:123], v132 offset:36864
	v_pk_add_f32 v[124:125], v[120:121], v[124:125]
	v_pk_add_f32 v[78:79], v[130:131], v[78:79]
	v_pk_add_f32 v[116:117], v[62:63], v[44:45]
	v_pk_add_f32 v[118:119], v[64:65], v[42:43]
	s_waitcnt lgkmcnt(3)
	v_mfma_f32_16x16x16_bf16 v[62:65], v[128:129], v[134:135], v[66:69]
	v_exp_f32_e32 v116, v116
	v_exp_f32_e32 v117, v117
	v_cvt_pk_bf16_f32 v128, v130, v131
	v_cvt_pk_bf16_f32 v129, v120, v121
	ds_read_b64_tr_b16 v[120:121], v132 offset:36928
	ds_read_b64_tr_b16 v[130:131], v132 offset:36936
	v_add_u32_e32 v132, v144, v104
	s_waitcnt lgkmcnt(4)
	v_mfma_f32_16x16x16_bf16 v[66:69], v[136:137], v[134:135], v[70:73]
	v_exp_f32_e32 v118, v118
	v_exp_f32_e32 v119, v119
	s_waitcnt lgkmcnt(2)
	v_mfma_f32_16x16x16_bf16 v[70:73], v[122:123], v[128:129], v[74:77]
	v_add_f32_e64 v122, v116, v124
	v_add_f32_e64 v123, v117, v125
	ds_read_b64_tr_b16 v[124:125], v132 offset:36872
	v_pk_add_f32 v[78:79], v[118:119], v[78:79]
	v_mfma_f32_16x16x16_bf16 v[74:77], v[126:127], v[128:129], v[112:115]
	v_cvt_pk_bf16_f32 v127, v116, v117
	v_cvt_pk_bf16_f32 v126, v118, v119
	s_nop 0
	v_pk_add_f32 v[112:113], v[58:59], v[44:45]
	v_pk_add_f32 v[114:115], v[60:61], v[42:43]
	s_waitcnt lgkmcnt(2)
	v_mfma_f32_16x16x16_bf16 v[58:61], v[120:121], v[128:129], v[62:65]
	ds_read_b64_tr_b16 v[120:121], v132 offset:36864
	v_exp_f32_e32 v112, v112
	v_exp_f32_e32 v113, v113
	v_exp_f32_e32 v114, v114
	s_waitcnt lgkmcnt(2)
	v_mfma_f32_16x16x16_bf16 v[62:65], v[130:131], v[128:129], v[66:69]
	ds_read_b64_tr_b16 v[116:117], v132 offset:36928
	ds_read_b64_tr_b16 v[128:129], v132 offset:36936
	v_exp_f32_e32 v115, v115
	v_pk_add_f32 v[118:119], v[112:113], v[122:123]
	v_add_u32_e32 v122, v144, v105
	s_waitcnt lgkmcnt(2)
	v_mfma_f32_16x16x16_bf16 v[66:69], v[120:121], v[126:127], v[70:73]
	ds_read_b64_tr_b16 v[120:121], v122 offset:36872
	v_mfma_f32_16x16x16_bf16 v[70:73], v[124:125], v[126:127], v[74:77]
	s_nop 2
	v_add_f32_e64 v74, v114, v78
	v_add_f32_e64 v75, v115, v79
	v_pk_add_f32 v[76:77], v[54:55], v[44:45]
	v_pk_add_f32 v[78:79], v[56:57], v[42:43]
	s_waitcnt lgkmcnt(2)
	v_mfma_f32_16x16x16_bf16 v[54:57], v[116:117], v[126:127], v[58:61]
	ds_read_b64_tr_b16 v[116:117], v122 offset:36864
	v_cvt_pk_bf16_f32 v114, v114, v115
	v_cvt_pk_bf16_f32 v115, v112, v113
	ds_read_b64_tr_b16 v[112:113], v122 offset:36928
	ds_read_b64_tr_b16 v[122:123], v122 offset:36936
	s_waitcnt lgkmcnt(4)
; #define LAS __attribute__((address_space(3)))
; __device__ __forceinline__ unsigned cvt_pk_bf16(float lo, float hi) { const f32x2_t v = {lo, hi}; return __builtin_bit_cast(unsigned, __builtin_convertvector(v, bf16x2_t)); }
; __device__ __forceinline__ s16x4 tr_read(LAS unsigned char* p) { return __builtin_bit_cast(s16x4, __builtin_amdgcn_ds_read_tr16_b64_v4i16((LAS s16x4*)p)); }
; __device__ __forceinline__ void phase_attn(Frame& F) {
;     ...
;         for (int T = 0; T < 9; ++T) {
;             u32x2 pw; pw.x = cvt_pk_bf16(St[T][0], St[T][1]); pw.y = cvt_pk_bf16(St[T][2], St[T][3]);
;             const s16x4 pb = __builtin_bit_cast(s16x4, pw);
;             LAS unsigned char* va = kb + ATT_VOFF + (16 * (w + T) + 4 * fq + (fr >> 2)) * ATT_ROWB + (8 * (fr & 3)) * 2;
; #pragma unroll
;             for (int dt = 0; dt < 4; ++dt) O[dt] = __builtin_amdgcn_mfma_f32_16x16x16bf16_1k(tr_read(va + 64 * (dt >> 1) + 8 * (dt & 1)), pb, O[dt], 0, 0, 0);
;         }
;         const float inv = 1.f / l;
;         bf16_t* op = (bf16_t*)((char*)part + (((size_t)cu.dsel * NTOK + (size_t)cu.b * SEQ + cu.r) * 512 + cu.h * 64) * 2 + (qrow * 1024u + 16u * fq));
; #pragma unroll
;         for (int u2 = 0; u2 < 2; ++u2) { u32x4 o4; o4.x = cvt_pk_bf16(O[2 * u2][0] * inv, O[2 * u2][1] * inv); o4.y = cvt_pk_bf16(O[2 * u2][2] * inv, O[2 * u2][3] * inv);
;             o4.z = cvt_pk_bf16(O[2 * u2 + 1][0] * inv, O[2 * u2 + 1][1] * inv); o4.w = cvt_pk_bf16(O[2 * u2 + 1][2] * inv, O[2 * u2 + 1][3] * inv); *(u32x4*)(op + 32 * u2) = o4; }
	v_mfma_f32_16x16x16_bf16 v[58:61], v[128:129], v[126:127], v[62:65]
	v_exp_f32_e32 v76, v76
	v_exp_f32_e32 v77, v77
	v_exp_f32_e32 v78, v78
	s_waitcnt lgkmcnt(2)
	v_mfma_f32_16x16x16_bf16 v[62:65], v[116:117], v[114:115], v[66:69]
	v_exp_f32_e32 v79, v79
	v_pk_add_f32 v[116:117], v[76:77], v[118:119]
	v_mfma_f32_16x16x16_bf16 v[66:69], v[120:121], v[114:115], v[70:73]
	s_nop 2
	v_add_f32_e64 v70, v42, v46
	v_add_f32_e64 v71, v43, v47
	s_waitcnt lgkmcnt(1)
	v_mfma_f32_16x16x16_bf16 v[42:45], v[112:113], v[114:115], v[54:57]
	v_exp_f32_e32 v72, v48
	v_exp_f32_e32 v73, v49
	v_exp_f32_e32 v70, v70
	v_add_u32_e32 v56, v144, v106
	ds_read_b64_tr_b16 v[54:55], v56 offset:36864
	s_waitcnt lgkmcnt(1)
	v_mfma_f32_16x16x16_bf16 v[46:49], v[122:123], v[114:115], v[58:61]
	v_exp_f32_e32 v71, v71
	v_cvt_pk_bf16_f32 v112, v78, v79
	v_cvt_pk_bf16_f32 v113, v76, v77
	ds_read_b64_tr_b16 v[58:59], v56 offset:36872
	ds_read_b64_tr_b16 v[76:77], v56 offset:36928
	ds_read_b64_tr_b16 v[114:115], v56 offset:36936
	s_waitcnt lgkmcnt(3)
	v_mfma_f32_16x16x16_bf16 v[54:57], v[54:55], v[112:113], v[62:65]
	s_nop 2
	v_add_f32_e64 v62, v78, v74
	v_add_f32_e64 v63, v79, v75
	v_pk_add_f32 v[64:65], v[72:73], v[116:117]
	v_pk_add_f32 v[62:63], v[70:71], v[62:63]
	v_add_u32_e32 v74, v144, v107
	s_waitcnt lgkmcnt(2)
	v_mfma_f32_16x16x16_bf16 v[58:61], v[58:59], v[112:113], v[66:69]
	s_nop 2
	v_pk_mov_b32 v[66:67], v[62:63], v[64:65] op_sel:[1,0]
	v_mov_b32_e32 v63, v65
	ds_read_b64_tr_b16 v[64:65], v74 offset:36864
	v_pk_add_f32 v[62:63], v[66:67], v[62:63]
	v_cvt_pk_bf16_f32 v66, v70, v71
	v_add_f32_e32 v75, v62, v63
	v_cvt_pk_bf16_f32 v67, v72, v73
	s_waitcnt lgkmcnt(2)
	v_mfma_f32_16x16x16_bf16 v[42:45], v[76:77], v[112:113], v[42:45]
	ds_read_b64_tr_b16 v[62:63], v74 offset:36872
	ds_read_b64_tr_b16 v[68:69], v74 offset:36928
	ds_read_b64_tr_b16 v[70:71], v74 offset:36936
	s_waitcnt lgkmcnt(3)
	v_mfma_f32_16x16x16_bf16 v[54:57], v[64:65], v[66:67], v[54:57]
	ds_bpermute_b32 v64, v142, v75
	s_waitcnt lgkmcnt(0)
	v_add_f32_e32 v72, v75, v64
	ds_bpermute_b32 v73, v143, v72
	v_mfma_f32_16x16x16_bf16 v[58:61], v[62:63], v[66:67], v[58:61]
	v_mfma_f32_16x16x16_bf16 v[62:65], v[68:69], v[66:67], v[42:45]
	s_waitcnt lgkmcnt(0)
	s_nop 1
	v_add_f32_e32 v43, v72, v73
	v_div_scale_f32 v68, s[64:65], v43, v43, 1.0
	v_mfma_f32_16x16x16_bf16 v[46:49], v[114:115], v[112:113], v[46:49]
	v_rcp_f32_e32 v69, v68
	v_lshlrev_b32_e32 v42, s35, v110
	s_ashr_i32 s35, s34, 31
	v_mfma_f32_16x16x16_bf16 v[44:47], v[70:71], v[66:67], v[46:49]
	s_lshl_b64 s[64:65], s[26:27], 16
	s_lshl_b64 s[34:35], s[34:35], 12
	s_ashr_i32 s26, s31, 31
	s_nop 0
	v_fma_f32 v48, -v68, v69, 1.0
	v_fmac_f32_e32 v69, v48, v69
	v_div_scale_f32 v48, vcc, 1.0, v43, 1.0
	v_mul_f32_e32 v49, v48, v69
	s_add_u32 s31, s34, s31
	v_fma_f32 v66, -v68, v49, v48
	s_addc_u32 s26, s35, s26
	v_fmac_f32_e32 v49, v66, v69
	s_add_u32 s34, s31, s64
	v_fma_f32 v48, -v68, v49, v48
	s_addc_u32 s35, s26, s65
	v_div_fmas_f32 v48, v48, v69, v49
	s_lshl_b32 s26, s30, 7
	s_lshl_b64 s[64:65], s[34:35], 10
	v_div_fixup_f32 v48, v48, v43, 1.0
	s_add_u32 s31, s24, s64
	v_lshl_or_b32 v49, v42, 10, v82
	s_addc_u32 s37, s25, s65
	v_pk_mul_f32 v[54:55], v[48:49], v[54:55] op_sel_hi:[0,1]
	v_pk_mul_f32 v[56:57], v[48:49], v[56:57] op_sel_hi:[0,1]
	s_add_u32 s64, s31, s26
	v_cvt_pk_bf16_f32 v54, v54, v55
	v_cvt_pk_bf16_f32 v55, v56, v57
	v_pk_mul_f32 v[56:57], v[48:49], v[58:59] op_sel_hi:[0,1]
	v_pk_mul_f32 v[58:59], v[48:49], v[60:61] op_sel_hi:[0,1]
	s_addc_u32 s65, s37, 0
	v_cvt_pk_bf16_f32 v56, v56, v57
	v_cvt_pk_bf16_f32 v57, v58, v59
	global_store_dwordx4 v49, v[54:57], s[64:65]
	v_pk_mul_f32 v[44:45], v[48:49], v[44:45] op_sel_hi:[0,1]
	s_nop 0
	v_pk_mul_f32 v[54:55], v[48:49], v[62:63] op_sel_hi:[0,1]
	v_pk_mul_f32 v[56:57], v[48:49], v[64:65] op_sel_hi:[0,1]
	v_cvt_pk_bf16_f32 v54, v54, v55
	v_cvt_pk_bf16_f32 v55, v56, v57
	v_cvt_pk_bf16_f32 v56, v44, v45
	v_pk_mul_f32 v[44:45], v[48:49], v[46:47] op_sel_hi:[0,1]
	v_cvt_pk_bf16_f32 v57, v44, v45
	global_store_dwordx4 v49, v[54:57], s[64:65] offset:64
	s_cmp_eq_u32 s95, 0
	s_cbranch_scc1 .Lcva_skip_l
; #define LAS __attribute__((address_space(3)))
; __device__ __forceinline__ void titem_finish(const TItem& t, int lane, const LAS unsigned char* buf) {
;     const int nblk = t.N / 32, kb = t.item / nblk, nb = t.item % nblk, k0 = 64 * kb, n0 = 32 * nb;
;     const int d0 = t.gmode == 0 ? n0 : ((n0 >> 7) * 256 + (n0 & 127) + (t.gmode == 2 ? 128 : 0));
;     const int c = lane & 7;
;     const LAS float* sb = (const LAS float*)buf;
;     float v[4][8];
;     const float wsc = t.scale;
; #pragma unroll
;     for (int j = 0; j < 4; ++j) { const int n = (lane >> 3) + 8 * j; const LAS float* s = sb + (8 * c) * 32 + 4 * ((n >> 2) ^ c) + (n & 3);
; #pragma unroll
;         for (int q = 0; q < 8; ++q) v[j][q] = s[32 * q] * wsc; }
;     if (t.f8) {
; #pragma unroll
;         for (int j = 0; j < 4; ++j) { const int n = (lane >> 3) + 8 * j;
;             int w0 = __builtin_amdgcn_cvt_pk_fp8_f32(v[j][0], v[j][1], 0, false); w0 = __builtin_amdgcn_cvt_pk_fp8_f32(v[j][2], v[j][3], w0, true);
;             int w1 = __builtin_amdgcn_cvt_pk_fp8_f32(v[j][4], v[j][5], 0, false); w1 = __builtin_amdgcn_cvt_pk_fp8_f32(v[j][6], v[j][7], w1, true);
;             u32x2 o; o.x = (unsigned)w0; o.y = (unsigned)w1;
;             __builtin_nontemporal_store(o, (u32x2*)((unsigned char*)t.WT + (size_t)(d0 + n) * t.K + k0 + 8 * c)); }
; __device__ __forceinline__ void phase_attn(Frame& F) {
;     ...
;         if (fq == 0) *(float*)((char*)lse + (((size_t)cu.dsel * NTOK + (size_t)cu.b * SEQ + cu.r) * 8 + cu.h) * 4 + qrow * 32u) = mx + __builtin_amdgcn_logf(l);
;         cu = nu; buf ^= 1;
	s_waitcnt vmcnt(12)
	v_pk_mul_f32 v[168:169], v[168:169], s[94:95] op_sel_hi:[1,0]
	v_pk_mul_f32 v[170:171], v[170:171], s[94:95] op_sel_hi:[1,0]
	v_pk_mul_f32 v[172:173], v[172:173], s[94:95] op_sel_hi:[1,0]
	v_pk_mul_f32 v[174:175], v[174:175], s[94:95] op_sel_hi:[1,0]
	v_pk_mul_f32 v[176:177], v[176:177], s[94:95] op_sel_hi:[1,0]
	v_pk_mul_f32 v[178:179], v[178:179], s[94:95] op_sel_hi:[1,0]
	v_pk_mul_f32 v[180:181], v[180:181], s[94:95] op_sel_hi:[1,0]
	v_pk_mul_f32 v[182:183], v[182:183], s[94:95] op_sel_hi:[1,0]
	v_pk_mul_f32 v[184:185], v[184:185], s[94:95] op_sel_hi:[1,0]
	v_pk_mul_f32 v[186:187], v[186:187], s[94:95] op_sel_hi:[1,0]
	v_pk_mul_f32 v[188:189], v[188:189], s[94:95] op_sel_hi:[1,0]
	v_pk_mul_f32 v[190:191], v[190:191], s[94:95] op_sel_hi:[1,0]
	v_pk_mul_f32 v[192:193], v[192:193], s[94:95] op_sel_hi:[1,0]
	v_pk_mul_f32 v[194:195], v[194:195], s[94:95] op_sel_hi:[1,0]
	v_pk_mul_f32 v[196:197], v[196:197], s[94:95] op_sel_hi:[1,0]
	v_pk_mul_f32 v[198:199], v[198:199], s[94:95] op_sel_hi:[1,0]
	v_pk_mul_f32 v[200:201], v[200:201], s[94:95] op_sel_hi:[1,0]
	v_pk_mul_f32 v[202:203], v[202:203], s[94:95] op_sel_hi:[1,0]
	v_pk_mul_f32 v[204:205], v[204:205], s[94:95] op_sel_hi:[1,0]
	v_pk_mul_f32 v[206:207], v[206:207], s[94:95] op_sel_hi:[1,0]
	v_pk_mul_f32 v[208:209], v[208:209], s[94:95] op_sel_hi:[1,0]
	v_pk_mul_f32 v[210:211], v[210:211], s[94:95] op_sel_hi:[1,0]
	v_pk_mul_f32 v[212:213], v[212:213], s[94:95] op_sel_hi:[1,0]
	v_pk_mul_f32 v[214:215], v[214:215], s[94:95] op_sel_hi:[1,0]
	v_pk_mul_f32 v[216:217], v[216:217], s[94:95] op_sel_hi:[1,0]
	v_pk_mul_f32 v[218:219], v[218:219], s[94:95] op_sel_hi:[1,0]
	v_pk_mul_f32 v[220:221], v[220:221], s[94:95] op_sel_hi:[1,0]
	v_pk_mul_f32 v[222:223], v[222:223], s[94:95] op_sel_hi:[1,0]
	v_pk_mul_f32 v[224:225], v[224:225], s[94:95] op_sel_hi:[1,0]
	v_pk_mul_f32 v[226:227], v[226:227], s[94:95] op_sel_hi:[1,0]
	v_pk_mul_f32 v[228:229], v[228:229], s[94:95] op_sel_hi:[1,0]
	v_pk_mul_f32 v[230:231], v[230:231], s[94:95] op_sel_hi:[1,0]
	s_lshr_b32 s99, s95, 2
	v_lshlrev_b32_e32 v250, 4, v248
	v_cvt_pk_fp8_f32 v232, v168, v172
	v_cvt_pk_fp8_f32 v233, v184, v188
	v_cvt_pk_fp8_f32 v234, v200, v204
	v_cvt_pk_fp8_f32 v235, v216, v220
	v_cvt_pk_fp8_f32 v236, v169, v173
	v_cvt_pk_fp8_f32 v237, v185, v189
	v_cvt_pk_fp8_f32 v238, v201, v205
	v_cvt_pk_fp8_f32 v239, v217, v221
	v_cvt_pk_fp8_f32 v240, v170, v174
	v_cvt_pk_fp8_f32 v241, v186, v190
	v_cvt_pk_fp8_f32 v242, v202, v206
	v_cvt_pk_fp8_f32 v243, v218, v222
	v_cvt_pk_fp8_f32 v244, v171, v175
	v_cvt_pk_fp8_f32 v245, v187, v191
	v_cvt_pk_fp8_f32 v246, v203, v207
	v_cvt_pk_fp8_f32 v247, v219, v223
	v_mad_u32_u24 v250, v249, s99, v250
	v_add_u32_e32 v251, s95, v250
	v_add_u32_e32 v254, s95, v251
	v_add_u32_e32 v255, s95, v254
	v_cvt_pk_fp8_f32 v232, v176, v180 op_sel:[0,0,1]
	v_cvt_pk_fp8_f32 v233, v192, v196 op_sel:[0,0,1]
	v_cvt_pk_fp8_f32 v234, v208, v212 op_sel:[0,0,1]
	v_cvt_pk_fp8_f32 v235, v224, v228 op_sel:[0,0,1]
	v_cvt_pk_fp8_f32 v236, v177, v181 op_sel:[0,0,1]
	v_cvt_pk_fp8_f32 v237, v193, v197 op_sel:[0,0,1]
	v_cvt_pk_fp8_f32 v238, v209, v213 op_sel:[0,0,1]
	v_cvt_pk_fp8_f32 v239, v225, v229 op_sel:[0,0,1]
	v_cvt_pk_fp8_f32 v240, v178, v182 op_sel:[0,0,1]
	v_cvt_pk_fp8_f32 v241, v194, v198 op_sel:[0,0,1]
	v_cvt_pk_fp8_f32 v242, v210, v214 op_sel:[0,0,1]
	v_cvt_pk_fp8_f32 v243, v226, v230 op_sel:[0,0,1]
	v_cvt_pk_fp8_f32 v244, v179, v183 op_sel:[0,0,1]
	v_cvt_pk_fp8_f32 v245, v195, v199 op_sel:[0,0,1]
	v_cvt_pk_fp8_f32 v246, v211, v215 op_sel:[0,0,1]
	v_cvt_pk_fp8_f32 v247, v227, v231 op_sel:[0,0,1]
	global_store_dwordx4 v250, v[232:235], s[92:93] nt
	global_store_dwordx4 v251, v[236:239], s[92:93] nt
	global_store_dwordx4 v254, v[240:243], s[92:93] nt
	global_store_dwordx4 v255, v[244:247], s[92:93] nt
.Lcva_skip_l:
	s_and_saveexec_b64 s[64:65], s[4:5]
	s_cbranch_execz .LBB0_303
	s_mov_b32 s31, s27
	v_log_f32_e32 v43, v43
	s_lshl_b64 s[34:35], s[34:35], 5
	s_lshl_b64 s[30:31], s[30:31], 2
	s_add_u32 s26, s67, s34
	s_addc_u32 s34, s68, s35
	s_add_u32 s30, s26, s30
	v_add_f32_e32 v43, v111, v43
	s_addc_u32 s31, s34, s31
	v_lshlrev_b32_e32 v42, 5, v42
	global_store_dword v42, v43, s[30:31]
	s_branch .LBB0_303
